# speedup vs baseline: 1.0047x; 1.0047x over previous
.LBB1_225:
	s_andn2_b64 vcc, exec, s[34:35]
	s_cbranch_vccnz .LBB1_222
	s_and_b64 s[34:35], s[30:31], exec
	s_cselect_b32 s20, 0, s46
	s_cselect_b32 s55, s5, s25
	s_cselect_b32 s56, s4, s24
	s_sub_i32 s20, s54, s20
	s_add_i32 s20, s20, 2
	s_lshl_b64 s[34:35], s[20:21], 7
	s_add_u32 s56, s56, s34
	s_addc_u32 s57, s55, s35
	s_and_b64 s[30:31], s[30:31], exec
	s_cselect_b32 s30, s0, s18
	s_cselect_b32 s20, s1, s19
	s_add_u32 s30, s30, s34
	s_addc_u32 s31, s20, s35
	s_add_i32 s20, s47, s51
	v_lshl_add_u64 v[154:155], s[30:31], 0, v[128:129]
	s_mov_b32 m0, s20
	s_nop 0
	global_load_lds_dwordx4 v[154:155], off
	v_lshl_add_u64 v[154:155], s[30:31], 0, v[132:133]
	s_add_i32 m0, s20, 0x2000
	s_nop 0
	global_load_lds_dwordx4 v[154:155], off
	s_add_i32 m0, s20, 0x4000
	v_lshl_add_u64 v[154:155], s[56:57], 0, v[130:131]
	global_load_lds_dwordx4 v[154:155], off
	s_add_i32 m0, s20, 0x6000
	s_add_u32 s30, s56, s6
	v_lshl_add_u64 v[154:155], s[56:57], 0, v[134:135]
	s_addc_u32 s31, s57, s7
	global_load_lds_dwordx4 v[154:155], off
	s_add_i32 m0, s20, 0x8000
	v_lshl_add_u64 v[154:155], s[30:31], 0, v[130:131]
	global_load_lds_dwordx4 v[154:155], off
	v_lshl_add_u64 v[154:155], s[30:31], 0, v[134:135]
	s_add_i32 m0, s20, 0xa000
	s_nop 0
	global_load_lds_dwordx4 v[154:155], off
	s_waitcnt vmcnt(7)
	s_branch .LBB1_222
